# speedup vs baseline: 1.0138x; 1.0018x over previous
.Lmfill_a:
	v_mov_b32_e32 v98, v241
	v_mov_b32_e32 v115, v241
	v_mov_b32_e32 v114, v241
	v_mov_b32_e32 v99, v241
	v_mov_b32_e32 v116, v241
	v_mov_b32_e32 v100, v241
	v_mov_b32_e32 v117, v241
	v_mov_b32_e32 v101, v241
	v_mov_b32_e32 v118, v241
	v_mov_b32_e32 v102, v241
	v_mov_b32_e32 v119, v241
	v_mov_b32_e32 v103, v241
	v_mov_b32_e32 v120, v241
	v_mov_b32_e32 v104, v241
	v_mov_b32_e32 v121, v241
	v_mov_b32_e32 v105, v241
	v_mov_b32_e32 v122, v241
	v_mov_b32_e32 v106, v241
	v_mov_b32_e32 v123, v241
	v_mov_b32_e32 v107, v241
	v_mov_b32_e32 v124, v241
	v_mov_b32_e32 v108, v241
	v_mov_b32_e32 v125, v241
	v_mov_b32_e32 v109, v241
	v_mov_b32_e32 v126, v241
	v_mov_b32_e32 v110, v241
	v_mov_b32_e32 v127, v241
	v_mov_b32_e32 v111, v241
	v_mov_b32_e32 v128, v241
	v_mov_b32_e32 v112, v241
	v_mov_b32_e32 v129, v241
	v_mov_b32_e32 v113, v241
	v_add_f32_e32 v242, v242, v94
	s_mov_b64 s[2:3], 0
	s_branch .LBB3_28

.Lmfill_b:
	v_mov_b32_e32 v66, v241
	v_mov_b32_e32 v83, v241
	v_mov_b32_e32 v82, v241
	v_mov_b32_e32 v67, v241
	v_mov_b32_e32 v84, v241
	v_mov_b32_e32 v68, v241
	v_mov_b32_e32 v85, v241
	v_mov_b32_e32 v69, v241
	v_mov_b32_e32 v86, v241
	v_mov_b32_e32 v70, v241
	v_mov_b32_e32 v87, v241
	v_mov_b32_e32 v71, v241
	v_mov_b32_e32 v88, v241
	v_mov_b32_e32 v72, v241
	v_mov_b32_e32 v89, v241
	v_mov_b32_e32 v73, v241
	v_mov_b32_e32 v90, v241
	v_mov_b32_e32 v74, v241
	v_mov_b32_e32 v91, v241
	v_mov_b32_e32 v75, v241
	v_mov_b32_e32 v92, v241
	v_mov_b32_e32 v76, v241
	v_mov_b32_e32 v93, v241
	v_mov_b32_e32 v77, v241
	v_mov_b32_e32 v94, v241
	v_mov_b32_e32 v78, v241
	v_mov_b32_e32 v95, v241
	v_mov_b32_e32 v79, v241
	v_mov_b32_e32 v96, v241
	v_mov_b32_e32 v80, v241
	v_mov_b32_e32 v97, v241
	v_mov_b32_e32 v81, v241
	v_add_f32_e32 v242, v242, v106
	s_mov_b64 s[28:29], 0
	s_branch .LBB3_39

.LBB3_72:
	v_add_u32_e32 v128, s43, v227
	ds_read_b64_tr_b16 v[118:119], v128 offset:24576
	ds_read_b64_tr_b16 v[120:121], v128 offset:25088
	v_add_f32_e32 v98, v82, v83
	v_add_f32_e32 v98, v84, v98
	v_add_f32_e32 v98, v85, v98
	v_add_f32_e32 v98, v86, v98
	v_add_f32_e32 v122, v87, v98
	s_waitcnt lgkmcnt(9)
	v_mfma_f32_32x32x16_f16 v[98:113], v[190:193], v[154:157], v[50:65]
	v_cvt_pk_f16_f32 v158, v82, v83
	v_cvt_pk_f16_f32 v159, v84, v85
	ds_read_b64_tr_b16 v[114:115], v128 offset:28672
	ds_read_b64_tr_b16 v[116:117], v128 offset:29184
	s_waitcnt lgkmcnt(10)
	v_mfma_f32_32x32x16_f16 v[50:65], v[186:189], v[154:157], v[50:65]
	v_add_f32_e32 v82, v88, v122
	v_add_f32_e32 v82, v89, v82
	v_add_f32_e32 v82, v90, v82
	v_add_f32_e32 v82, v91, v82
	v_cvt_pk_f16_f32 v160, v86, v87
	v_cvt_pk_f16_f32 v161, v88, v89
	ds_read_b64_tr_b16 v[122:123], v128 offset:25600
	ds_read_b64_tr_b16 v[124:125], v128 offset:26112
	s_waitcnt lgkmcnt(11)
	v_mfma_f32_32x32x16_f16 v[98:113], v[182:185], v[146:149], v[98:113]
	v_add_f32_e32 v82, v92, v82
	v_add_f32_e32 v82, v93, v82
	v_add_f32_e32 v82, v94, v82
	v_add_f32_e32 v82, v95, v82
	v_cvt_pk_f16_f32 v150, v90, v91
	v_cvt_pk_f16_f32 v151, v92, v93
	ds_read_b64_tr_b16 v[182:183], v128 offset:29696
	ds_read_b64_tr_b16 v[184:185], v128 offset:30208
	s_waitcnt lgkmcnt(12)
	v_mfma_f32_32x32x16_f16 v[50:65], v[178:181], v[146:149], v[50:65]
	v_add_f32_e32 v82, v96, v82
	v_add_f32_e32 v82, v97, v82
	v_add_f32_e32 v82, v66, v82
	v_add_f32_e32 v82, v67, v82
	v_cvt_pk_f16_f32 v152, v94, v95
	v_cvt_pk_f16_f32 v153, v96, v97
	ds_read_b64_tr_b16 v[154:155], v128 offset:26624
	ds_read_b64_tr_b16 v[156:157], v128 offset:27136
	s_waitcnt lgkmcnt(13)
	v_mfma_f32_32x32x16_f16 v[98:113], v[174:177], v[138:141], v[98:113]
	v_add_f32_e32 v82, v68, v82
	v_add_f32_e32 v82, v69, v82
	v_add_f32_e32 v82, v70, v82
	v_add_f32_e32 v82, v71, v82
	v_cvt_pk_f16_f32 v142, v66, v67
	v_cvt_pk_f16_f32 v143, v68, v69
	ds_read_b64_tr_b16 v[146:147], v128 offset:30720
	ds_read_b64_tr_b16 v[148:149], v128 offset:31232
	s_waitcnt lgkmcnt(14)
	v_mfma_f32_32x32x16_f16 v[50:65], v[170:173], v[138:141], v[50:65]
	v_add_f32_e32 v66, v72, v82
	v_add_f32_e32 v66, v73, v66
	v_add_f32_e32 v66, v74, v66
	v_add_f32_e32 v66, v75, v66
	v_cvt_pk_f16_f32 v144, v70, v71
	v_cvt_pk_f16_f32 v145, v72, v73
	ds_read_b64_tr_b16 v[138:139], v128 offset:27648
	ds_read_b64_tr_b16 v[140:141], v128 offset:28160
	s_waitcnt lgkmcnt(14)
	v_mfma_f32_32x32x16_f16 v[98:113], v[166:169], v[130:133], v[98:113]
	v_add_f32_e32 v66, v76, v66
	v_add_f32_e32 v66, v77, v66
	v_add_f32_e32 v66, v78, v66
	v_add_f32_e32 v66, v79, v66
	v_cvt_pk_f16_f32 v134, v74, v75
	v_cvt_pk_f16_f32 v135, v76, v77
	ds_read_b64_tr_b16 v[126:127], v128 offset:31744
	ds_read_b64_tr_b16 v[128:129], v128 offset:32256
	v_mfma_f32_32x32x16_f16 v[50:65], v[162:165], v[130:133], v[50:65]
	v_add_f32_e32 v66, v80, v66
	v_add_f32_e32 v66, v81, v66
	v_add_f32_e32 v82, 0, v66
	v_cvt_pk_f16_f32 v136, v78, v79
	v_cvt_pk_f16_f32 v137, v80, v81
	s_cmp_lt_u32 s35, 6
	s_cbranch_scc0 .Lmpart_c
	v_add_f32_e32 v98, v242, v82
	v_mov_b32_e32 v66, v241
	v_mov_b32_e32 v67, v241
	v_mov_b32_e32 v68, v241
	v_mov_b32_e32 v69, v241
	v_mov_b32_e32 v70, v241
	v_mov_b32_e32 v71, v241
	v_mov_b32_e32 v72, v241
	v_mov_b32_e32 v73, v241
	v_mov_b32_e32 v74, v241
	v_mov_b32_e32 v75, v241
	v_mov_b32_e32 v76, v241
	v_mov_b32_e32 v77, v241
	v_mov_b32_e32 v78, v241
	v_mov_b32_e32 v79, v241
	v_mov_b32_e32 v80, v241
	v_mov_b32_e32 v81, v241
	v_mov_b32_e32 v50, v241
	v_mov_b32_e32 v51, v241
	v_mov_b32_e32 v52, v241
	v_mov_b32_e32 v53, v241
	v_mov_b32_e32 v54, v241
	v_mov_b32_e32 v55, v241
	v_mov_b32_e32 v56, v241
	v_mov_b32_e32 v57, v241
	v_mov_b32_e32 v58, v241
	v_mov_b32_e32 v59, v241
	v_mov_b32_e32 v60, v241
	v_mov_b32_e32 v61, v241
	v_mov_b32_e32 v62, v241
	v_mov_b32_e32 v63, v241
	v_mov_b32_e32 v64, v241
	v_mov_b32_e32 v65, v241
	s_mov_b64 s[2:3], 0
	s_branch .LBB3_73
.Lmpart_c:
	v_or_b32_e32 v66, 0xe0, v228
	v_cmp_le_u32_e32 vcc, v66, v219
	v_or_b32_e32 v68, 0xe1, v228
	v_or_b32_e32 v69, 0xe2, v228
	s_nop 2
	v_cndmask_b32_e32 v50, v241, v50, vcc
	v_cmp_lt_u32_e32 vcc, v230, v219
	v_or_b32_e32 v70, 0xe3, v228
	v_or_b32_e32 v71, 0xe8, v228
	v_cndmask_b32_e32 v67, v241, v99, vcc
	v_cmp_le_u32_e32 vcc, v230, v219
	v_or_b32_e32 v72, 0xe9, v228
	v_or_b32_e32 v73, 0xea, v228
	v_cndmask_b32_e32 v66, v241, v98, vcc
	v_cmp_le_u32_e32 vcc, v68, v219
	v_or_b32_e32 v68, 0xc2, v228
	v_or_b32_e32 v74, 0xeb, v228
	v_cndmask_b32_e32 v51, v241, v51, vcc
	v_cmp_le_u32_e32 vcc, v68, v219
	v_or_b32_e32 v75, 0xf0, v228
	v_or_b32_e32 v76, 0xf1, v228
	v_cndmask_b32_e32 v68, v241, v100, vcc
	v_cmp_le_u32_e32 vcc, v69, v219
	v_or_b32_e32 v69, 0xc3, v228
	v_or_b32_e32 v77, 0xf2, v228
	v_cndmask_b32_e32 v52, v241, v52, vcc
	v_cmp_le_u32_e32 vcc, v69, v219
	v_or_b32_e32 v78, 0xf3, v228
	v_or_b32_e32 v79, 0xf8, v228
	v_cndmask_b32_e32 v69, v241, v101, vcc
	v_cmp_le_u32_e32 vcc, v70, v219
	v_or_b32_e32 v70, 0xc8, v228
	v_or_b32_e32 v80, 0xf9, v228
	v_cndmask_b32_e32 v53, v241, v53, vcc
	v_cmp_le_u32_e32 vcc, v70, v219
	v_or_b32_e32 v81, 0xfa, v228
	v_or_b32_e32 v83, 0xfb, v228
	v_cndmask_b32_e32 v70, v241, v102, vcc
	v_cmp_le_u32_e32 vcc, v71, v219
	v_or_b32_e32 v71, 0xc9, v228
	v_max_f32_e32 v84, v66, v66
	v_cndmask_b32_e32 v54, v241, v54, vcc
	v_cmp_le_u32_e32 vcc, v71, v219
	v_add_f32_e32 v98, v242, v82
	s_nop 0
	v_cndmask_b32_e32 v71, v241, v103, vcc
	v_cmp_le_u32_e32 vcc, v72, v219
	v_or_b32_e32 v72, 0xca, v228
	s_nop 0
	v_cndmask_b32_e32 v55, v241, v55, vcc
	v_cmp_le_u32_e32 vcc, v72, v219
	s_nop 1
	v_cndmask_b32_e32 v72, v241, v104, vcc
	v_cmp_le_u32_e32 vcc, v73, v219
	v_or_b32_e32 v73, 0xcb, v228
	s_nop 0
	v_cndmask_b32_e32 v56, v241, v56, vcc
	v_cmp_le_u32_e32 vcc, v73, v219
	s_nop 1
	v_cndmask_b32_e32 v73, v241, v105, vcc
	v_cmp_le_u32_e32 vcc, v74, v219
	v_or_b32_e32 v74, 0xd0, v228
	s_nop 0
	v_cndmask_b32_e32 v57, v241, v57, vcc
	v_cmp_le_u32_e32 vcc, v74, v219
	s_nop 1
	v_cndmask_b32_e32 v74, v241, v106, vcc
	v_cmp_le_u32_e32 vcc, v75, v219
	v_or_b32_e32 v75, 0xd1, v228
	s_nop 0
	v_cndmask_b32_e32 v58, v241, v58, vcc
	v_cmp_le_u32_e32 vcc, v75, v219
	s_nop 1
	v_cndmask_b32_e32 v75, v241, v107, vcc
	v_cmp_le_u32_e32 vcc, v76, v219
	v_or_b32_e32 v76, 0xd2, v228
	s_nop 0
	v_cndmask_b32_e32 v59, v241, v59, vcc
	v_cmp_le_u32_e32 vcc, v76, v219
	s_nop 1
	v_cndmask_b32_e32 v76, v241, v108, vcc
	v_cmp_le_u32_e32 vcc, v77, v219
	v_or_b32_e32 v77, 0xd3, v228
	s_nop 0
	v_cndmask_b32_e32 v60, v241, v60, vcc
	v_cmp_le_u32_e32 vcc, v77, v219
	s_nop 1
	v_cndmask_b32_e32 v77, v241, v109, vcc
	v_cmp_le_u32_e32 vcc, v78, v219
	v_or_b32_e32 v78, 0xd8, v228
	s_nop 0
	v_cndmask_b32_e32 v61, v241, v61, vcc
	v_cmp_le_u32_e32 vcc, v78, v219
	s_nop 1
	v_cndmask_b32_e32 v78, v241, v110, vcc
	v_cmp_le_u32_e32 vcc, v79, v219
	v_or_b32_e32 v79, 0xd9, v228
	s_nop 0
	v_cndmask_b32_e32 v62, v241, v62, vcc
	v_cmp_le_u32_e32 vcc, v79, v219
	s_nop 1
	v_cndmask_b32_e32 v79, v241, v111, vcc
	v_cmp_le_u32_e32 vcc, v80, v219
	v_or_b32_e32 v80, 0xda, v228
	s_nop 0
	v_cndmask_b32_e32 v63, v241, v63, vcc
	v_cmp_le_u32_e32 vcc, v80, v219
	s_nop 1
	v_cndmask_b32_e32 v80, v241, v112, vcc
	v_cmp_le_u32_e32 vcc, v81, v219
	v_or_b32_e32 v81, 0xdb, v228
	s_nop 0
	v_cndmask_b32_e32 v64, v241, v64, vcc
	v_cmp_le_u32_e32 vcc, v81, v219
	s_nop 1
	v_cndmask_b32_e32 v81, v241, v113, vcc
	v_cmp_le_u32_e32 vcc, v83, v219
	v_max_f32_e32 v83, v67, v67
	v_max_f32_e32 v83, v84, v83
	v_max3_f32 v84, v68, v69, v51
	v_max3_f32 v83, v83, v50, v52
	v_max3_f32 v83, v83, v53, v70
	v_max3_f32 v84, v84, v72, v73
	v_max3_f32 v83, v83, v71, v54
	v_max3_f32 v84, v84, v56, v57
	v_max3_f32 v83, v83, v55, v74
	v_max3_f32 v84, v84, v76, v77
	v_max3_f32 v83, v83, v75, v58
	v_max3_f32 v84, v84, v60, v61
	v_cndmask_b32_e32 v65, v241, v65, vcc
	v_max3_f32 v83, v83, v59, v78
	v_max3_f32 v84, v84, v80, v81
	v_max3_f32 v83, v83, v79, v62
	v_max3_f32 v84, v84, v64, v65
	v_max3_f32 v82, v83, v63, v84
	v_mov_b32_e32 v83, v82
	s_nop 1
	v_permlane32_swap_b32_e32 v82, v83
	v_max_f32_e32 v82, v82, v83
	v_cmp_lt_f32_e32 vcc, s34, v82
	s_cmp_lg_u64 vcc, 0
	s_cselect_b64 s[2:3], -1, 0
	s_cbranch_vccnz .LBB3_77
